# P6/P7 epilogues: 39 dead zero-initialisations of fp8 pack registers dropped (both halves are written by the convert pair before any read), on top of v95
# speedup vs baseline: 1.0059x; 1.0059x over previous
.LBB0_783:
	s_nop 15
	s_nop 15
	s_waitcnt vmcnt(0)
	v_pk_mul_f32 v[8:9], v[6:7], s[20:21] op_sel_hi:[1,0]
	v_pk_mul_f32 v[10:11], v[4:5], s[20:21] op_sel_hi:[1,0]
	v_pk_mul_f32 v[6:7], v[12:13], s[20:21] op_sel_hi:[1,0]
	v_pk_mul_f32 v[4:5], v[14:15], s[20:21] op_sel_hi:[1,0]
	v_pk_fma_f32 v[158:159], v[158:159], s[22:23], v[10:11] op_sel_hi:[1,0,1]
	v_pk_fma_f32 v[154:155], v[154:155], s[22:23], v[6:7] op_sel_hi:[1,0,1]
	v_pk_fma_f32 v[156:157], v[156:157], s[22:23], v[4:5] op_sel_hi:[1,0,1]
	v_pk_add_f32 v[16:17], v[26:27], 1.0 op_sel_hi:[1,0]
	v_pk_add_f32 v[18:19], v[24:25], 1.0 op_sel_hi:[1,0]
	v_min_f32_e32 v24, 0x42600000, v158
	v_min_f32_e32 v26, 0x42600000, v154
	v_min_f32_e32 v25, 0x42600000, v159
	v_min_f32_e32 v27, 0x42600000, v155
	v_pk_add_f32 v[12:13], v[30:31], 1.0 op_sel_hi:[1,0]
	v_min_f32_e32 v31, 0x42600000, v157
	v_mul_f32_e32 v23, 0xbe9d265f, v24
	v_mul_f32_e32 v155, 0xbe9d265f, v26
	v_mul_f32_e32 v157, 0xbe9d265f, v25
	v_mul_f32_e32 v158, 0xbe9d265f, v27
	v_min_f32_e32 v30, 0x42600000, v156
	v_exp_f32_e32 v154, v23
	v_exp_f32_e32 v156, v155
	v_exp_f32_e32 v155, v157
	v_exp_f32_e32 v157, v158
	v_pk_fma_f32 v[160:161], v[160:161], s[22:23], v[8:9] op_sel_hi:[1,0,1]
	v_pk_add_f32 v[14:15], v[28:29], 1.0 op_sel_hi:[1,0]
	v_min_f32_e32 v28, 0x42600000, v160
	v_min_f32_e32 v29, 0x42600000, v161
	v_pk_fma_f32 v[144:145], v[144:145], s[24:25], v[16:17] op_sel_hi:[1,0,1]
	v_pk_fma_f32 v[140:141], v[140:141], s[24:25], v[12:13] op_sel_hi:[1,0,1]
	v_mul_f32_e32 v159, 0xbe9d265f, v28
	v_mul_f32_e32 v160, 0xbe9d265f, v30
	v_mul_f32_e32 v161, 0xbe9d265f, v29
	v_mul_f32_e32 v171, 0xbe9d265f, v31
	v_med3_f32 v144, v144, s76, v213
	v_med3_f32 v140, v140, s76, v213
	v_med3_f32 v145, v145, s76, v213
	v_med3_f32 v141, v141, s76, v213
	v_exp_f32_e32 v158, v159
	v_exp_f32_e32 v160, v160
	v_exp_f32_e32 v159, v161
	v_exp_f32_e32 v161, v171
	v_pk_mul_f32 v[28:29], v[28:29], v[144:145]
	v_pk_mul_f32 v[30:31], v[30:31], v[140:141]
	v_pk_add_f32 v[140:141], v[154:155], 1.0 op_sel_hi:[1,0]
	v_pk_add_f32 v[144:145], v[156:157], 1.0 op_sel_hi:[1,0]
	v_rcp_f32_e32 v140, v140
	v_rcp_f32_e32 v144, v144
	v_rcp_f32_e32 v141, v141
	v_rcp_f32_e32 v145, v145
	v_pk_fma_f32 v[142:143], v[142:143], s[24:25], v[18:19] op_sel_hi:[1,0,1]
	v_pk_fma_f32 v[138:139], v[138:139], s[24:25], v[14:15] op_sel_hi:[1,0,1]
	v_med3_f32 v142, v142, s76, v213
	v_med3_f32 v138, v138, s76, v213
	v_med3_f32 v143, v143, s76, v213
	v_med3_f32 v139, v139, s76, v213
	v_pk_mul_f32 v[24:25], v[24:25], v[142:143]
	v_pk_mul_f32 v[26:27], v[26:27], v[138:139]
	v_pk_add_f32 v[138:139], v[158:159], 1.0 op_sel_hi:[1,0]
	v_pk_add_f32 v[142:143], v[160:161], 1.0 op_sel_hi:[1,0]
	v_rcp_f32_e32 v138, v138
	v_rcp_f32_e32 v142, v142
	v_rcp_f32_e32 v139, v139
	v_rcp_f32_e32 v143, v143
	v_pk_mul_f32 v[24:25], v[24:25], v[140:141]
	v_pk_mul_f32 v[26:27], v[26:27], v[144:145]
	v_cvt_pk_fp8_f32 v32, v24, v25
	v_cvt_pk_fp8_f32 v33, v26, v27
	v_pk_mul_f32 v[24:25], v[28:29], v[138:139]
	v_pk_mul_f32 v[26:27], v[30:31], v[142:143]
	v_cvt_pk_fp8_f32 v32, v24, v25 op_sel:[0,0,1]
	v_cvt_pk_fp8_f32 v33, v26, v27 op_sel:[0,0,1]
	v_pk_fma_f32 v[152:153], v[152:153], s[22:23], v[8:9] op_sel_hi:[1,0,1]
	v_pk_fma_f32 v[150:151], v[150:151], s[22:23], v[10:11] op_sel_hi:[1,0,1]
	v_pk_fma_f32 v[148:149], v[148:149], s[22:23], v[4:5] op_sel_hi:[1,0,1]
	v_pk_fma_f32 v[146:147], v[146:147], s[22:23], v[6:7] op_sel_hi:[1,0,1]
	v_min_f32_e32 v150, 0x42600000, v150
	v_pk_fma_f32 v[134:135], v[134:135], s[24:25], v[18:19] op_sel_hi:[1,0,1]
	v_min_f32_e32 v28, 0x42600000, v152
	v_min_f32_e32 v146, 0x42600000, v146
	v_pk_fma_f32 v[136:137], v[136:137], s[24:25], v[16:17] op_sel_hi:[1,0,1]
	v_pk_fma_f32 v[132:133], v[132:133], s[24:25], v[12:13] op_sel_hi:[1,0,1]
	v_med3_f32 v27, v135, s76, v213
	v_min_f32_e32 v30, 0x42600000, v148
	v_mul_f32_e32 v23, 0xbe9d265f, v150
	v_mul_f32_e32 v135, 0xbe9d265f, v28
	v_pk_fma_f32 v[24:25], v[130:131], s[24:25], v[14:15] op_sel_hi:[1,0,1]
	global_store_dwordx2 v[2:3], v[32:33], off
	v_min_f32_e32 v151, 0x42600000, v151
	v_med3_f32 v32, v136, s76, v213
	v_med3_f32 v130, v132, s76, v213
	v_min_f32_e32 v29, 0x42600000, v153
	v_exp_f32_e32 v132, v23
	v_mul_f32_e32 v23, 0xbe9d265f, v146
	v_exp_f32_e32 v136, v135
	v_mul_f32_e32 v135, 0xbe9d265f, v30
	v_med3_f32 v26, v134, s76, v213
	v_min_f32_e32 v147, 0x42600000, v147
	v_min_f32_e32 v31, 0x42600000, v149
	v_exp_f32_e32 v134, v23
	v_mul_f32_e32 v23, 0xbe9d265f, v151
	v_exp_f32_e32 v138, v135
	v_mul_f32_e32 v135, 0xbe9d265f, v29
	v_med3_f32 v33, v137, s76, v213
	v_med3_f32 v131, v133, s76, v213
	v_exp_f32_e32 v133, v23
	v_mul_f32_e32 v23, 0xbe9d265f, v147
	v_exp_f32_e32 v137, v135
	v_mul_f32_e32 v135, 0xbe9d265f, v31
	v_exp_f32_e32 v139, v135
	v_exp_f32_e32 v135, v23
	v_pk_add_f32 v[132:133], v[132:133], 1.0 op_sel_hi:[1,0]
	v_med3_f32 v24, v24, s76, v213
	v_rcp_f32_e32 v132, v132
	v_pk_add_f32 v[134:135], v[134:135], 1.0 op_sel_hi:[1,0]
	v_rcp_f32_e32 v133, v133
	v_rcp_f32_e32 v134, v134
	v_rcp_f32_e32 v135, v135
	v_med3_f32 v25, v25, s76, v213
	v_pk_add_f32 v[138:139], v[138:139], 1.0 op_sel_hi:[1,0]
	v_pk_mul_f32 v[24:25], v[146:147], v[24:25]
	v_pk_add_f32 v[136:137], v[136:137], 1.0 op_sel_hi:[1,0]
	v_rcp_f32_e32 v138, v138
	v_rcp_f32_e32 v139, v139
	v_pk_mul_f32 v[28:29], v[28:29], v[32:33]
	v_pk_mul_f32 v[26:27], v[150:151], v[26:27]
	v_pk_mul_f32 v[24:25], v[24:25], v[134:135]
	v_rcp_f32_e32 v136, v136
	v_rcp_f32_e32 v137, v137
	v_pk_mul_f32 v[26:27], v[26:27], v[132:133]
	v_cvt_pk_fp8_f32 v33, v24, v25
	v_cvt_pk_fp8_f32 v32, v26, v27
	v_pk_mul_f32 v[24:25], v[30:31], v[130:131]
	v_pk_mul_f32 v[28:29], v[28:29], v[136:137]
	v_pk_mul_f32 v[24:25], v[24:25], v[138:139]
	v_cvt_pk_fp8_f32 v32, v28, v29 op_sel:[0,0,1]
	v_cvt_pk_fp8_f32 v33, v24, v25 op_sel:[0,0,1]
	v_or_b32_e32 v24, 16, v22
	v_ashrrev_i32_e32 v25, 31, v24
	v_lshlrev_b64 v[24:25], 11, v[24:25]
	v_lshl_add_u64 v[24:25], s[14:15], 0, v[24:25]
	v_lshl_add_u64 v[24:25], v[24:25], 0, v[20:21]
	global_store_dwordx2 v[24:25], v[32:33], off
	v_pk_fma_f32 v[24:25], v[128:129], s[22:23], v[8:9] op_sel_hi:[1,0,1]
	v_pk_fma_f32 v[26:27], v[126:127], s[22:23], v[10:11] op_sel_hi:[1,0,1]
	v_pk_fma_f32 v[28:29], v[124:125], s[22:23], v[4:5] op_sel_hi:[1,0,1]
	v_pk_fma_f32 v[30:31], v[122:123], s[22:23], v[6:7] op_sel_hi:[1,0,1]
	v_min_f32_e32 v26, 0x42600000, v26
	v_min_f32_e32 v24, 0x42600000, v24
	v_min_f32_e32 v30, 0x42600000, v30
	v_min_f32_e32 v28, 0x42600000, v28
	v_mul_f32_e32 v23, 0xbe9d265f, v26
	v_mul_f32_e32 v123, 0xbe9d265f, v24
	v_pk_fma_f32 v[32:33], v[120:121], s[24:25], v[16:17] op_sel_hi:[1,0,1]
	v_min_f32_e32 v27, 0x42600000, v27
	v_min_f32_e32 v25, 0x42600000, v25
	v_exp_f32_e32 v120, v23
	v_mul_f32_e32 v23, 0xbe9d265f, v30
	v_exp_f32_e32 v124, v123
	v_mul_f32_e32 v123, 0xbe9d265f, v28
	v_min_f32_e32 v31, 0x42600000, v31
	v_min_f32_e32 v29, 0x42600000, v29
	v_exp_f32_e32 v122, v23
	v_mul_f32_e32 v23, 0xbe9d265f, v27
	v_exp_f32_e32 v126, v123
	v_mul_f32_e32 v123, 0xbe9d265f, v25
	v_exp_f32_e32 v121, v23
	v_mul_f32_e32 v23, 0xbe9d265f, v31
	v_exp_f32_e32 v125, v123
	v_mul_f32_e32 v123, 0xbe9d265f, v29
	v_exp_f32_e32 v127, v123
	v_exp_f32_e32 v123, v23
	v_pk_add_f32 v[120:121], v[120:121], 1.0 op_sel_hi:[1,0]
	v_pk_fma_f32 v[118:119], v[118:119], s[24:25], v[18:19] op_sel_hi:[1,0,1]
	v_rcp_f32_e32 v120, v120
	v_pk_add_f32 v[122:123], v[122:123], 1.0 op_sel_hi:[1,0]
	v_rcp_f32_e32 v121, v121
	v_rcp_f32_e32 v122, v122
	v_rcp_f32_e32 v123, v123
	v_pk_fma_f32 v[114:115], v[114:115], s[24:25], v[14:15] op_sel_hi:[1,0,1]
	v_med3_f32 v118, v118, s76, v213
	v_med3_f32 v119, v119, s76, v213
	v_med3_f32 v114, v114, s76, v213
	v_med3_f32 v115, v115, s76, v213
	v_med3_f32 v32, v32, s76, v213
	v_med3_f32 v33, v33, s76, v213
	v_pk_add_f32 v[124:125], v[124:125], 1.0 op_sel_hi:[1,0]
	v_pk_mul_f32 v[26:27], v[26:27], v[118:119]
	v_pk_add_f32 v[126:127], v[126:127], 1.0 op_sel_hi:[1,0]
	v_rcp_f32_e32 v124, v124
	v_rcp_f32_e32 v125, v125
	v_pk_mul_f32 v[24:25], v[24:25], v[32:33]
	v_pk_mul_f32 v[26:27], v[26:27], v[120:121]
	v_pk_mul_f32 v[30:31], v[30:31], v[114:115]
	v_rcp_f32_e32 v126, v126
	v_rcp_f32_e32 v127, v127
	v_pk_mul_f32 v[30:31], v[30:31], v[122:123]
	v_cvt_pk_fp8_f32 v32, v26, v27
	v_pk_fma_f32 v[116:117], v[116:117], s[24:25], v[12:13] op_sel_hi:[1,0,1]
	v_cvt_pk_fp8_f32 v33, v30, v31
	v_med3_f32 v116, v116, s76, v213
	v_med3_f32 v117, v117, s76, v213
	v_pk_mul_f32 v[24:25], v[24:25], v[124:125]
	v_pk_mul_f32 v[26:27], v[28:29], v[116:117]
	v_cvt_pk_fp8_f32 v32, v24, v25 op_sel:[0,0,1]
	v_pk_mul_f32 v[26:27], v[26:27], v[126:127]
	v_or_b32_e32 v24, 32, v22
	v_cvt_pk_fp8_f32 v33, v26, v27 op_sel:[0,0,1]
	v_ashrrev_i32_e32 v25, 31, v24
	v_lshlrev_b64 v[24:25], 11, v[24:25]
	v_lshl_add_u64 v[24:25], s[14:15], 0, v[24:25]
	v_lshl_add_u64 v[24:25], v[24:25], 0, v[20:21]
	global_store_dwordx2 v[24:25], v[32:33], off
	v_pk_fma_f32 v[24:25], v[112:113], s[22:23], v[8:9] op_sel_hi:[1,0,1]
	v_pk_fma_f32 v[26:27], v[110:111], s[22:23], v[10:11] op_sel_hi:[1,0,1]
	v_pk_fma_f32 v[28:29], v[108:109], s[22:23], v[4:5] op_sel_hi:[1,0,1]
	v_pk_fma_f32 v[30:31], v[106:107], s[22:23], v[6:7] op_sel_hi:[1,0,1]
	v_min_f32_e32 v26, 0x42600000, v26
	v_min_f32_e32 v24, 0x42600000, v24
	v_min_f32_e32 v30, 0x42600000, v30
	v_min_f32_e32 v28, 0x42600000, v28
	v_mul_f32_e32 v23, 0xbe9d265f, v26
	v_mul_f32_e32 v107, 0xbe9d265f, v24
	v_pk_fma_f32 v[32:33], v[104:105], s[24:25], v[16:17] op_sel_hi:[1,0,1]
	v_min_f32_e32 v27, 0x42600000, v27
	v_min_f32_e32 v25, 0x42600000, v25
	v_exp_f32_e32 v104, v23
	v_mul_f32_e32 v23, 0xbe9d265f, v30
	v_exp_f32_e32 v108, v107
	v_mul_f32_e32 v107, 0xbe9d265f, v28
	v_min_f32_e32 v31, 0x42600000, v31
	v_min_f32_e32 v29, 0x42600000, v29
	v_exp_f32_e32 v106, v23
	v_mul_f32_e32 v23, 0xbe9d265f, v27
	v_exp_f32_e32 v110, v107
	v_mul_f32_e32 v107, 0xbe9d265f, v25
	v_exp_f32_e32 v105, v23
	v_mul_f32_e32 v23, 0xbe9d265f, v31
	v_exp_f32_e32 v109, v107
	v_mul_f32_e32 v107, 0xbe9d265f, v29
	v_exp_f32_e32 v111, v107
	v_exp_f32_e32 v107, v23
	v_pk_add_f32 v[104:105], v[104:105], 1.0 op_sel_hi:[1,0]
	v_pk_fma_f32 v[102:103], v[102:103], s[24:25], v[18:19] op_sel_hi:[1,0,1]
	v_rcp_f32_e32 v104, v104
	v_pk_add_f32 v[106:107], v[106:107], 1.0 op_sel_hi:[1,0]
	v_rcp_f32_e32 v105, v105
	v_rcp_f32_e32 v106, v106
	v_rcp_f32_e32 v107, v107
	v_pk_fma_f32 v[98:99], v[98:99], s[24:25], v[14:15] op_sel_hi:[1,0,1]
	v_med3_f32 v102, v102, s76, v213
	v_med3_f32 v98, v98, s76, v213
	v_med3_f32 v103, v103, s76, v213
	v_med3_f32 v99, v99, s76, v213
	v_med3_f32 v32, v32, s76, v213
	v_med3_f32 v33, v33, s76, v213
	v_pk_add_f32 v[108:109], v[108:109], 1.0 op_sel_hi:[1,0]
	v_pk_add_f32 v[110:111], v[110:111], 1.0 op_sel_hi:[1,0]
	v_pk_mul_f32 v[26:27], v[26:27], v[102:103]
	v_pk_mul_f32 v[30:31], v[30:31], v[98:99]
	v_rcp_f32_e32 v108, v108
	v_rcp_f32_e32 v110, v110
	v_rcp_f32_e32 v109, v109
	v_rcp_f32_e32 v111, v111
	v_pk_mul_f32 v[24:25], v[24:25], v[32:33]
	v_pk_mul_f32 v[26:27], v[26:27], v[104:105]
	v_pk_mul_f32 v[30:31], v[30:31], v[106:107]
	v_pk_fma_f32 v[100:101], v[100:101], s[24:25], v[12:13] op_sel_hi:[1,0,1]
	v_cvt_pk_fp8_f32 v32, v26, v27
	v_cvt_pk_fp8_f32 v33, v30, v31
	v_med3_f32 v100, v100, s76, v213
	v_med3_f32 v101, v101, s76, v213
	v_pk_mul_f32 v[26:27], v[28:29], v[100:101]
	v_pk_mul_f32 v[24:25], v[24:25], v[108:109]
	v_pk_mul_f32 v[26:27], v[26:27], v[110:111]
	v_or_b32_e32 v22, 48, v22
	v_cvt_pk_fp8_f32 v32, v24, v25 op_sel:[0,0,1]
	v_cvt_pk_fp8_f32 v33, v26, v27 op_sel:[0,0,1]
	v_ashrrev_i32_e32 v23, 31, v22
	v_lshlrev_b64 v[22:23], 11, v[22:23]
	v_lshl_add_u64 v[22:23], s[14:15], 0, v[22:23]
	v_pk_fma_f32 v[26:27], v[90:91], s[22:23], v[6:7] op_sel_hi:[1,0,1]
	v_lshl_add_u64 v[20:21], v[22:23], 0, v[20:21]
	v_pk_fma_f32 v[22:23], v[94:95], s[22:23], v[10:11] op_sel_hi:[1,0,1]
	v_min_f32_e32 v26, 0x42600000, v26
	global_store_dwordx2 v[20:21], v[32:33], off
	v_pk_fma_f32 v[32:33], v[84:85], s[24:25], v[12:13] op_sel_hi:[1,0,1]
	v_min_f32_e32 v22, 0x42600000, v22
	v_min_f32_e32 v23, 0x42600000, v23
	v_min_f32_e32 v27, 0x42600000, v27
	v_mul_f32_e32 v85, 0xbe9d265f, v26
	v_pk_fma_f32 v[30:31], v[86:87], s[24:25], v[18:19] op_sel_hi:[1,0,1]
	v_mul_f32_e32 v84, 0xbe9d265f, v22
	v_exp_f32_e32 v86, v85
	v_mul_f32_e32 v85, 0xbe9d265f, v23
	v_mul_f32_e32 v87, 0xbe9d265f, v27
	v_pk_fma_f32 v[24:25], v[92:93], s[22:23], v[4:5] op_sel_hi:[1,0,1]
	v_exp_f32_e32 v84, v84
	v_exp_f32_e32 v85, v85
	v_exp_f32_e32 v87, v87
	v_pk_fma_f32 v[20:21], v[96:97], s[22:23], v[8:9] op_sel_hi:[1,0,1]
	v_min_f32_e32 v24, 0x42600000, v24
	v_pk_fma_f32 v[28:29], v[88:89], s[24:25], v[16:17] op_sel_hi:[1,0,1]
	v_min_f32_e32 v20, 0x42600000, v20
	v_min_f32_e32 v21, 0x42600000, v21
	v_min_f32_e32 v25, 0x42600000, v25
	v_mul_f32_e32 v89, 0xbe9d265f, v24
	v_mul_f32_e32 v88, 0xbe9d265f, v20
	v_exp_f32_e32 v90, v89
	v_mul_f32_e32 v89, 0xbe9d265f, v21
	v_mul_f32_e32 v91, 0xbe9d265f, v25
	v_exp_f32_e32 v88, v88
	v_exp_f32_e32 v89, v89
	v_exp_f32_e32 v91, v91
	v_pk_add_f32 v[84:85], v[84:85], 1.0 op_sel_hi:[1,0]
	v_pk_add_f32 v[86:87], v[86:87], 1.0 op_sel_hi:[1,0]
	v_rcp_f32_e32 v84, v84
	v_rcp_f32_e32 v86, v86
	v_rcp_f32_e32 v85, v85
	v_rcp_f32_e32 v87, v87
	v_pk_fma_f32 v[82:83], v[82:83], s[24:25], v[14:15] op_sel_hi:[1,0,1]
	v_med3_f32 v30, v30, s76, v213
	v_med3_f32 v82, v82, s76, v213
	v_med3_f32 v31, v31, s76, v213
	v_med3_f32 v83, v83, s76, v213
	v_med3_f32 v28, v28, s76, v213
	v_med3_f32 v29, v29, s76, v213
	v_pk_add_f32 v[88:89], v[88:89], 1.0 op_sel_hi:[1,0]
	v_pk_add_f32 v[90:91], v[90:91], 1.0 op_sel_hi:[1,0]
	v_pk_mul_f32 v[22:23], v[22:23], v[30:31]
	v_pk_mul_f32 v[26:27], v[26:27], v[82:83]
	v_rcp_f32_e32 v88, v88
	v_rcp_f32_e32 v90, v90
	v_rcp_f32_e32 v89, v89
	v_rcp_f32_e32 v91, v91
	v_pk_mul_f32 v[20:21], v[20:21], v[28:29]
	v_pk_mul_f32 v[22:23], v[22:23], v[84:85]
	v_pk_mul_f32 v[26:27], v[26:27], v[86:87]
	v_cvt_pk_fp8_f32 v28, v22, v23
	v_cvt_pk_fp8_f32 v29, v26, v27
	v_med3_f32 v32, v32, s76, v213
	v_med3_f32 v33, v33, s76, v213
	v_pk_mul_f32 v[22:23], v[24:25], v[32:33]
	v_pk_mul_f32 v[20:21], v[20:21], v[88:89]
	v_pk_mul_f32 v[22:23], v[22:23], v[90:91]
	v_pk_fma_f32 v[26:27], v[74:75], s[22:23], v[6:7] op_sel_hi:[1,0,1]
	v_cvt_pk_fp8_f32 v28, v20, v21 op_sel:[0,0,1]
	v_cvt_pk_fp8_f32 v29, v22, v23 op_sel:[0,0,1]
	v_pk_fma_f32 v[22:23], v[78:79], s[22:23], v[10:11] op_sel_hi:[1,0,1]
	v_min_f32_e32 v26, 0x42600000, v26
	v_pk_fma_f32 v[32:33], v[68:69], s[24:25], v[12:13] op_sel_hi:[1,0,1]
	v_min_f32_e32 v22, 0x42600000, v22
	v_min_f32_e32 v23, 0x42600000, v23
	v_min_f32_e32 v27, 0x42600000, v27
	v_mul_f32_e32 v69, 0xbe9d265f, v26
	v_add_co_u32_e32 v20, vcc, s77, v2
	v_pk_fma_f32 v[30:31], v[70:71], s[24:25], v[18:19] op_sel_hi:[1,0,1]
	v_mul_f32_e32 v68, 0xbe9d265f, v22
	v_exp_f32_e32 v70, v69
	v_mul_f32_e32 v69, 0xbe9d265f, v23
	v_mul_f32_e32 v71, 0xbe9d265f, v27
	v_addc_co_u32_e32 v21, vcc, 0, v3, vcc
	v_pk_fma_f32 v[24:25], v[76:77], s[22:23], v[4:5] op_sel_hi:[1,0,1]
	v_exp_f32_e32 v68, v68
	v_exp_f32_e32 v69, v69
	v_exp_f32_e32 v71, v71
	global_store_dwordx2 v[20:21], v[28:29], off
	v_pk_fma_f32 v[20:21], v[80:81], s[22:23], v[8:9] op_sel_hi:[1,0,1]
	v_min_f32_e32 v24, 0x42600000, v24
	v_pk_fma_f32 v[28:29], v[72:73], s[24:25], v[16:17] op_sel_hi:[1,0,1]
	v_min_f32_e32 v20, 0x42600000, v20
	v_min_f32_e32 v21, 0x42600000, v21
	v_min_f32_e32 v25, 0x42600000, v25
	v_mul_f32_e32 v73, 0xbe9d265f, v24
	v_mul_f32_e32 v72, 0xbe9d265f, v20
	v_exp_f32_e32 v74, v73
	v_mul_f32_e32 v73, 0xbe9d265f, v21
	v_mul_f32_e32 v75, 0xbe9d265f, v25
	v_exp_f32_e32 v72, v72
	v_exp_f32_e32 v73, v73
	v_exp_f32_e32 v75, v75
	v_pk_add_f32 v[68:69], v[68:69], 1.0 op_sel_hi:[1,0]
	v_pk_add_f32 v[70:71], v[70:71], 1.0 op_sel_hi:[1,0]
	v_rcp_f32_e32 v68, v68
	v_rcp_f32_e32 v70, v70
	v_rcp_f32_e32 v69, v69
	v_rcp_f32_e32 v71, v71
	v_pk_fma_f32 v[66:67], v[66:67], s[24:25], v[14:15] op_sel_hi:[1,0,1]
	v_med3_f32 v30, v30, s76, v213
	v_med3_f32 v66, v66, s76, v213
	v_med3_f32 v31, v31, s76, v213
	v_med3_f32 v67, v67, s76, v213
	v_med3_f32 v28, v28, s76, v213
	v_med3_f32 v29, v29, s76, v213
	v_pk_add_f32 v[72:73], v[72:73], 1.0 op_sel_hi:[1,0]
	v_pk_add_f32 v[74:75], v[74:75], 1.0 op_sel_hi:[1,0]
	v_pk_mul_f32 v[22:23], v[22:23], v[30:31]
	v_pk_mul_f32 v[26:27], v[26:27], v[66:67]
	v_rcp_f32_e32 v72, v72
	v_rcp_f32_e32 v74, v74
	v_rcp_f32_e32 v73, v73
	v_rcp_f32_e32 v75, v75
	v_pk_mul_f32 v[20:21], v[20:21], v[28:29]
	v_pk_mul_f32 v[22:23], v[22:23], v[68:69]
	v_pk_mul_f32 v[26:27], v[26:27], v[70:71]
	v_cvt_pk_fp8_f32 v28, v22, v23
	v_cvt_pk_fp8_f32 v29, v26, v27
	v_med3_f32 v32, v32, s76, v213
	v_med3_f32 v33, v33, s76, v213
	v_pk_mul_f32 v[22:23], v[24:25], v[32:33]
	v_pk_mul_f32 v[20:21], v[20:21], v[72:73]
	v_pk_mul_f32 v[22:23], v[22:23], v[74:75]
	v_pk_fma_f32 v[26:27], v[58:59], s[22:23], v[6:7] op_sel_hi:[1,0,1]
	v_cvt_pk_fp8_f32 v28, v20, v21 op_sel:[0,0,1]
	v_cvt_pk_fp8_f32 v29, v22, v23 op_sel:[0,0,1]
	v_pk_fma_f32 v[22:23], v[62:63], s[22:23], v[10:11] op_sel_hi:[1,0,1]
	v_min_f32_e32 v26, 0x42600000, v26
	v_pk_fma_f32 v[32:33], v[52:53], s[24:25], v[12:13] op_sel_hi:[1,0,1]
	v_min_f32_e32 v22, 0x42600000, v22
	v_min_f32_e32 v23, 0x42600000, v23
	v_min_f32_e32 v27, 0x42600000, v27
	v_mul_f32_e32 v53, 0xbe9d265f, v26
	v_add_co_u32_e32 v20, vcc, s78, v2
	v_pk_fma_f32 v[30:31], v[54:55], s[24:25], v[18:19] op_sel_hi:[1,0,1]
	v_mul_f32_e32 v52, 0xbe9d265f, v22
	v_exp_f32_e32 v54, v53
	v_mul_f32_e32 v53, 0xbe9d265f, v23
	v_mul_f32_e32 v55, 0xbe9d265f, v27
	v_addc_co_u32_e32 v21, vcc, 0, v3, vcc
	v_pk_fma_f32 v[24:25], v[60:61], s[22:23], v[4:5] op_sel_hi:[1,0,1]
	v_exp_f32_e32 v52, v52
	v_exp_f32_e32 v53, v53
	v_exp_f32_e32 v55, v55
	global_store_dwordx2 v[20:21], v[28:29], off
	v_pk_fma_f32 v[20:21], v[64:65], s[22:23], v[8:9] op_sel_hi:[1,0,1]
	v_min_f32_e32 v24, 0x42600000, v24
	v_pk_fma_f32 v[28:29], v[56:57], s[24:25], v[16:17] op_sel_hi:[1,0,1]
	v_min_f32_e32 v20, 0x42600000, v20
	v_min_f32_e32 v21, 0x42600000, v21
	v_min_f32_e32 v25, 0x42600000, v25
	v_mul_f32_e32 v57, 0xbe9d265f, v24
	v_mul_f32_e32 v56, 0xbe9d265f, v20
	v_exp_f32_e32 v58, v57
	v_mul_f32_e32 v57, 0xbe9d265f, v21
	v_mul_f32_e32 v59, 0xbe9d265f, v25
	v_exp_f32_e32 v56, v56
	v_exp_f32_e32 v57, v57
	v_exp_f32_e32 v59, v59
	v_pk_add_f32 v[52:53], v[52:53], 1.0 op_sel_hi:[1,0]
	v_pk_add_f32 v[54:55], v[54:55], 1.0 op_sel_hi:[1,0]
	v_rcp_f32_e32 v52, v52
	v_rcp_f32_e32 v54, v54
	v_rcp_f32_e32 v53, v53
	v_rcp_f32_e32 v55, v55
	v_pk_fma_f32 v[50:51], v[50:51], s[24:25], v[14:15] op_sel_hi:[1,0,1]
	v_med3_f32 v30, v30, s76, v213
	v_med3_f32 v50, v50, s76, v213
	v_med3_f32 v31, v31, s76, v213
	v_med3_f32 v51, v51, s76, v213
	v_med3_f32 v28, v28, s76, v213
	v_med3_f32 v29, v29, s76, v213
	v_pk_add_f32 v[56:57], v[56:57], 1.0 op_sel_hi:[1,0]
	v_pk_add_f32 v[58:59], v[58:59], 1.0 op_sel_hi:[1,0]
	v_pk_mul_f32 v[22:23], v[22:23], v[30:31]
	v_pk_mul_f32 v[26:27], v[26:27], v[50:51]
	v_rcp_f32_e32 v56, v56
	v_rcp_f32_e32 v58, v58
	v_rcp_f32_e32 v57, v57
	v_rcp_f32_e32 v59, v59
	v_pk_mul_f32 v[20:21], v[20:21], v[28:29]
	v_pk_mul_f32 v[22:23], v[22:23], v[52:53]
	v_pk_mul_f32 v[26:27], v[26:27], v[54:55]
	v_cvt_pk_fp8_f32 v28, v22, v23
	v_cvt_pk_fp8_f32 v29, v26, v27
	v_med3_f32 v32, v32, s76, v213
	v_med3_f32 v33, v33, s76, v213
	v_pk_mul_f32 v[22:23], v[24:25], v[32:33]
	v_pk_mul_f32 v[20:21], v[20:21], v[56:57]
	v_pk_mul_f32 v[22:23], v[22:23], v[58:59]
	v_cvt_pk_fp8_f32 v28, v20, v21 op_sel:[0,0,1]
	v_cvt_pk_fp8_f32 v29, v22, v23 op_sel:[0,0,1]
	v_add_co_u32_e32 v20, vcc, s79, v2
	v_pk_fma_f32 v[6:7], v[42:43], s[22:23], v[6:7] op_sel_hi:[1,0,1]
	s_nop 0
	v_addc_co_u32_e32 v21, vcc, 0, v3, vcc
	v_pk_fma_f32 v[10:11], v[46:47], s[22:23], v[10:11] op_sel_hi:[1,0,1]
	v_min_f32_e32 v6, 0x42600000, v6
	global_store_dwordx2 v[20:21], v[28:29], off
	v_min_f32_e32 v10, 0x42600000, v10
	v_min_f32_e32 v11, 0x42600000, v11
	v_min_f32_e32 v7, 0x42600000, v7
	v_mul_f32_e32 v21, 0xbe9d265f, v6
	v_mul_f32_e32 v20, 0xbe9d265f, v10
	v_exp_f32_e32 v22, v21
	v_mul_f32_e32 v21, 0xbe9d265f, v11
	v_mul_f32_e32 v23, 0xbe9d265f, v7
	v_pk_fma_f32 v[4:5], v[44:45], s[22:23], v[4:5] op_sel_hi:[1,0,1]
	v_exp_f32_e32 v20, v20
	v_exp_f32_e32 v21, v21
	v_exp_f32_e32 v23, v23
	v_pk_fma_f32 v[8:9], v[48:49], s[22:23], v[8:9] op_sel_hi:[1,0,1]
	v_min_f32_e32 v4, 0x42600000, v4
	v_min_f32_e32 v8, 0x42600000, v8
	v_min_f32_e32 v9, 0x42600000, v9
	v_min_f32_e32 v5, 0x42600000, v5
	v_mul_f32_e32 v25, 0xbe9d265f, v4
	v_mul_f32_e32 v24, 0xbe9d265f, v8
	v_exp_f32_e32 v26, v25
	v_mul_f32_e32 v25, 0xbe9d265f, v9
	v_mul_f32_e32 v27, 0xbe9d265f, v5
	v_exp_f32_e32 v24, v24
	v_exp_f32_e32 v25, v25
	v_exp_f32_e32 v27, v27
	v_pk_add_f32 v[20:21], v[20:21], 1.0 op_sel_hi:[1,0]
	v_pk_add_f32 v[22:23], v[22:23], 1.0 op_sel_hi:[1,0]
	v_rcp_f32_e32 v20, v20
	v_rcp_f32_e32 v22, v22
	v_rcp_f32_e32 v21, v21
	v_rcp_f32_e32 v23, v23
	v_pk_fma_f32 v[18:19], v[38:39], s[24:25], v[18:19] op_sel_hi:[1,0,1]
	v_pk_fma_f32 v[14:15], v[34:35], s[24:25], v[14:15] op_sel_hi:[1,0,1]
	v_med3_f32 v18, v18, s76, v213
	v_med3_f32 v14, v14, s76, v213
	v_med3_f32 v19, v19, s76, v213
	v_med3_f32 v15, v15, s76, v213
	v_pk_add_f32 v[24:25], v[24:25], 1.0 op_sel_hi:[1,0]
	v_pk_add_f32 v[26:27], v[26:27], 1.0 op_sel_hi:[1,0]
	v_pk_mul_f32 v[10:11], v[10:11], v[18:19]
	v_pk_mul_f32 v[6:7], v[6:7], v[14:15]
	v_rcp_f32_e32 v24, v24
	v_rcp_f32_e32 v26, v26
	v_rcp_f32_e32 v25, v25
	v_rcp_f32_e32 v27, v27
	v_pk_mul_f32 v[10:11], v[10:11], v[20:21]
	v_pk_mul_f32 v[6:7], v[6:7], v[22:23]
	v_pk_fma_f32 v[16:17], v[40:41], s[24:25], v[16:17] op_sel_hi:[1,0,1]
	v_pk_fma_f32 v[12:13], v[36:37], s[24:25], v[12:13] op_sel_hi:[1,0,1]
	v_cvt_pk_fp8_f32 v14, v10, v11
	v_cvt_pk_fp8_f32 v15, v6, v7
	v_med3_f32 v16, v16, s76, v213
	v_med3_f32 v12, v12, s76, v213
	v_med3_f32 v17, v17, s76, v213
	v_med3_f32 v13, v13, s76, v213
	v_pk_mul_f32 v[8:9], v[8:9], v[16:17]
	v_pk_mul_f32 v[4:5], v[4:5], v[12:13]
	v_pk_mul_f32 v[8:9], v[8:9], v[24:25]
	v_pk_mul_f32 v[4:5], v[4:5], v[26:27]
	v_cvt_pk_fp8_f32 v14, v8, v9 op_sel:[0,0,1]
	v_cvt_pk_fp8_f32 v15, v4, v5 op_sel:[0,0,1]
	v_add_co_u32_e32 v2, vcc, 0x58000, v2
	s_nop 1
	v_addc_co_u32_e32 v3, vcc, 0, v3, vcc
	s_andn2_b64 vcc, exec, s[98:99]
	global_store_dwordx2 v[2:3], v[14:15], off
	s_cbranch_vccnz .LBB0_786
	s_branch .Lp6_entry_pre

.LBB0_868:
	s_nop 15
	s_nop 15
	s_waitcnt vmcnt(0)
	v_pk_mul_f32 v[30:31], v[10:11], s[22:23] op_sel_hi:[1,0]
	s_nop 0
	v_pk_fma_f32 v[32:33], v[158:159], s[24:25], v[30:31] op_sel_hi:[1,0,1]
	v_pk_mul_f32 v[12:13], v[12:13], s[22:23] op_sel_hi:[1,0]
	v_med3_f32 v21, v32, s74, v215
	v_med3_f32 v29, v33, s74, v215
	v_cvt_pk_fp8_f32 v22, v21, v29
	v_pk_mul_f32 v[14:15], v[14:15], s[22:23] op_sel_hi:[1,0]
	v_pk_fma_f32 v[10:11], v[160:161], s[24:25], v[12:13] op_sel_hi:[1,0,1]
	v_pk_fma_f32 v[130:131], v[130:131], s[24:25], v[14:15] op_sel_hi:[1,0,1]
	v_med3_f32 v10, v10, s74, v215
	v_med3_f32 v11, v11, s74, v215
	v_pk_fma_f32 v[154:155], v[154:155], s[24:25], v[14:15] op_sel_hi:[1,0,1]
	v_med3_f32 v130, v130, s74, v215
	v_cvt_pk_fp8_f32 v22, v10, v11 op_sel:[0,0,1]
	v_med3_f32 v10, v131, s74, v215
	ds_bpermute_b32 v22, v250, v22
	v_pk_fma_f32 v[150:151], v[150:151], s[24:25], v[30:31] op_sel_hi:[1,0,1]
	v_pk_fma_f32 v[146:147], v[146:147], s[24:25], v[14:15] op_sel_hi:[1,0,1]
	v_med3_f32 v32, v154, s74, v215
	v_med3_f32 v33, v155, s74, v215
	v_cvt_pk_fp8_f32 v29, v130, v10
	v_pk_mul_f32 v[16:17], v[16:17], s[22:23] op_sel_hi:[1,0]
	v_pk_fma_f32 v[142:143], v[142:143], s[24:25], v[30:31] op_sel_hi:[1,0,1]
	v_pk_fma_f32 v[138:139], v[138:139], s[24:25], v[14:15] op_sel_hi:[1,0,1]
	v_med3_f32 v150, v150, s74, v215
	v_med3_f32 v151, v151, s74, v215
	v_med3_f32 v146, v146, s74, v215
	v_med3_f32 v147, v147, s74, v215
	v_cvt_pk_fp8_f32 v23, v32, v33
	v_pk_fma_f32 v[132:133], v[132:133], s[24:25], v[16:17] op_sel_hi:[1,0,1]
	v_med3_f32 v142, v142, s74, v215
	v_med3_f32 v143, v143, s74, v215
	v_med3_f32 v138, v138, s74, v215
	v_med3_f32 v139, v139, s74, v215
	v_cvt_pk_fp8_f32 v24, v150, v151
	v_cvt_pk_fp8_f32 v25, v146, v147
	v_pk_fma_f32 v[156:157], v[156:157], s[24:25], v[16:17] op_sel_hi:[1,0,1]
	v_cvt_pk_fp8_f32 v26, v142, v143
	v_cvt_pk_fp8_f32 v27, v138, v139
	v_med3_f32 v10, v132, s74, v215
	v_med3_f32 v11, v133, s74, v215
	v_pk_fma_f32 v[152:153], v[152:153], s[24:25], v[12:13] op_sel_hi:[1,0,1]
	v_pk_fma_f32 v[148:149], v[148:149], s[24:25], v[16:17] op_sel_hi:[1,0,1]
	v_med3_f32 v154, v156, s74, v215
	v_med3_f32 v155, v157, s74, v215
	v_cvt_pk_fp8_f32 v29, v10, v11 op_sel:[0,0,1]
	v_or_b32_e32 v10, 48, v20
	ds_bpermute_b32 v29, v250, v29
	v_pk_fma_f32 v[144:145], v[144:145], s[24:25], v[12:13] op_sel_hi:[1,0,1]
	v_pk_fma_f32 v[140:141], v[140:141], s[24:25], v[16:17] op_sel_hi:[1,0,1]
	v_med3_f32 v152, v152, s74, v215
	v_med3_f32 v153, v153, s74, v215
	v_med3_f32 v148, v148, s74, v215
	v_med3_f32 v149, v149, s74, v215
	v_cvt_pk_fp8_f32 v23, v154, v155 op_sel:[0,0,1]
	v_ashrrev_i32_e32 v11, 31, v10
	ds_bpermute_b32 v23, v250, v23
	v_med3_f32 v144, v144, s74, v215
	v_med3_f32 v145, v145, s74, v215
	v_med3_f32 v140, v140, s74, v215
	v_med3_f32 v141, v141, s74, v215
	v_cvt_pk_fp8_f32 v24, v152, v153 op_sel:[0,0,1]
	v_cvt_pk_fp8_f32 v25, v148, v149 op_sel:[0,0,1]
	ds_bpermute_b32 v24, v250, v24
	v_lshlrev_b64 v[10:11], 11, v[10:11]
	ds_bpermute_b32 v25, v250, v25
	v_cvt_pk_fp8_f32 v26, v144, v145 op_sel:[0,0,1]
	v_cvt_pk_fp8_f32 v27, v140, v141 op_sel:[0,0,1]
	ds_bpermute_b32 v26, v250, v26
	v_lshl_add_u64 v[10:11], s[16:17], 0, v[10:11]
	ds_bpermute_b32 v27, v250, v27
	v_lshl_add_u64 v[10:11], v[10:11], 0, v[18:19]
	v_lshl_add_u64 v[10:11], v[10:11], 0, v[202:203]
	v_pk_fma_f32 v[18:19], v[128:129], s[24:25], v[12:13] op_sel_hi:[1,0,1]
	v_pk_fma_f32 v[20:21], v[126:127], s[24:25], v[30:31] op_sel_hi:[1,0,1]
	s_waitcnt lgkmcnt(0)
	global_store_dwordx2 v[4:5], v[22:23], off
	global_store_dwordx2 v[6:7], v[24:25], off
	global_store_dwordx2 v[8:9], v[26:27], off
	v_pk_fma_f32 v[24:25], v[122:123], s[24:25], v[14:15] op_sel_hi:[1,0,1]
	v_med3_f32 v20, v20, s74, v215
	v_med3_f32 v21, v21, s74, v215
	v_med3_f32 v26, v18, s74, v215
	v_med3_f32 v27, v19, s74, v215
	v_cvt_pk_fp8_f32 v18, v20, v21
	v_med3_f32 v20, v24, s74, v215
	v_med3_f32 v21, v25, s74, v215
	v_cvt_pk_fp8_f32 v19, v20, v21
	v_pk_fma_f32 v[22:23], v[124:125], s[24:25], v[16:17] op_sel_hi:[1,0,1]
	v_cvt_pk_fp8_f32 v18, v26, v27 op_sel:[0,0,1]
	v_med3_f32 v20, v22, s74, v215
	ds_bpermute_b32 v18, v250, v18
	v_med3_f32 v21, v23, s74, v215
	v_cvt_pk_fp8_f32 v19, v20, v21 op_sel:[0,0,1]
	v_add_co_u32_e32 v20, vcc, s75, v4
	ds_bpermute_b32 v19, v250, v19
	v_pk_fma_f32 v[24:25], v[114:115], s[24:25], v[14:15] op_sel_hi:[1,0,1]
	s_nop 0
	v_addc_co_u32_e32 v21, vcc, 0, v5, vcc
	s_waitcnt lgkmcnt(0)
	global_store_dwordx2 v[20:21], v[18:19], off
	v_pk_fma_f32 v[18:19], v[120:121], s[24:25], v[12:13] op_sel_hi:[1,0,1]
	v_pk_fma_f32 v[20:21], v[118:119], s[24:25], v[30:31] op_sel_hi:[1,0,1]
	v_med3_f32 v26, v18, s74, v215
	v_med3_f32 v20, v20, s74, v215
	v_med3_f32 v21, v21, s74, v215
	v_med3_f32 v27, v19, s74, v215
	v_cvt_pk_fp8_f32 v18, v20, v21
	v_med3_f32 v20, v24, s74, v215
	v_med3_f32 v21, v25, s74, v215
	v_cvt_pk_fp8_f32 v19, v20, v21
	v_pk_fma_f32 v[22:23], v[116:117], s[24:25], v[16:17] op_sel_hi:[1,0,1]
	v_cvt_pk_fp8_f32 v18, v26, v27 op_sel:[0,0,1]
	v_med3_f32 v20, v22, s74, v215
	ds_bpermute_b32 v18, v250, v18
	v_med3_f32 v21, v23, s74, v215
	v_cvt_pk_fp8_f32 v19, v20, v21 op_sel:[0,0,1]
	v_add_co_u32_e32 v20, vcc, s76, v4
	ds_bpermute_b32 v19, v250, v19
	v_pk_fma_f32 v[24:25], v[106:107], s[24:25], v[14:15] op_sel_hi:[1,0,1]
	s_nop 0
	v_addc_co_u32_e32 v21, vcc, 0, v5, vcc
	s_waitcnt lgkmcnt(0)
	global_store_dwordx2 v[20:21], v[18:19], off
	v_pk_fma_f32 v[18:19], v[112:113], s[24:25], v[12:13] op_sel_hi:[1,0,1]
	v_pk_fma_f32 v[20:21], v[110:111], s[24:25], v[30:31] op_sel_hi:[1,0,1]
	v_med3_f32 v26, v18, s74, v215
	v_med3_f32 v20, v20, s74, v215
	v_med3_f32 v21, v21, s74, v215
	v_med3_f32 v27, v19, s74, v215
	v_cvt_pk_fp8_f32 v18, v20, v21
	v_med3_f32 v20, v24, s74, v215
	v_med3_f32 v21, v25, s74, v215
	v_cvt_pk_fp8_f32 v19, v20, v21
	v_pk_fma_f32 v[22:23], v[108:109], s[24:25], v[16:17] op_sel_hi:[1,0,1]
	v_cvt_pk_fp8_f32 v18, v26, v27 op_sel:[0,0,1]
	v_med3_f32 v20, v22, s74, v215
	ds_bpermute_b32 v18, v250, v18
	v_med3_f32 v21, v23, s74, v215
	v_cvt_pk_fp8_f32 v19, v20, v21 op_sel:[0,0,1]
	v_add_co_u32_e32 v20, vcc, s77, v4
	ds_bpermute_b32 v19, v250, v19
	v_pk_fma_f32 v[136:137], v[136:137], s[24:25], v[12:13] op_sel_hi:[1,0,1]
	s_nop 0
	v_addc_co_u32_e32 v21, vcc, 0, v5, vcc
	v_pk_fma_f32 v[134:135], v[134:135], s[24:25], v[30:31] op_sel_hi:[1,0,1]
	s_waitcnt lgkmcnt(0)
	global_store_dwordx2 v[20:21], v[18:19], off
	v_pk_fma_f32 v[12:13], v[100:101], s[24:25], v[12:13] op_sel_hi:[1,0,1]
	v_pk_fma_f32 v[18:19], v[98:99], s[24:25], v[30:31] op_sel_hi:[1,0,1]
	v_pk_fma_f32 v[14:15], v[90:91], s[24:25], v[14:15] op_sel_hi:[1,0,1]
	v_med3_f32 v134, v134, s74, v215
	v_med3_f32 v135, v135, s74, v215
	v_med3_f32 v18, v18, s74, v215
	v_med3_f32 v19, v19, s74, v215
	v_med3_f32 v20, v12, s74, v215
	v_med3_f32 v21, v13, s74, v215
	v_med3_f32 v14, v14, s74, v215
	v_med3_f32 v15, v15, s74, v215
	v_cvt_pk_fp8_f32 v28, v134, v135
	v_cvt_pk_fp8_f32 v12, v18, v19
	v_cvt_pk_fp8_f32 v13, v14, v15
	v_pk_fma_f32 v[16:17], v[92:93], s[24:25], v[16:17] op_sel_hi:[1,0,1]
	v_med3_f32 v136, v136, s74, v215
	v_med3_f32 v137, v137, s74, v215
	v_med3_f32 v14, v16, s74, v215
	v_med3_f32 v15, v17, s74, v215
	v_cvt_pk_fp8_f32 v28, v136, v137 op_sel:[0,0,1]
	v_cvt_pk_fp8_f32 v12, v20, v21 op_sel:[0,0,1]
	ds_bpermute_b32 v28, v250, v28
	v_cvt_pk_fp8_f32 v13, v14, v15 op_sel:[0,0,1]
	ds_bpermute_b32 v12, v250, v12
	v_add_co_u32_e32 v14, vcc, s78, v4
	ds_bpermute_b32 v13, v250, v13
	s_waitcnt lgkmcnt(0)
	global_store_dwordx2 v[10:11], v[28:29], off
	s_nop 0
	v_addc_co_u32_e32 v15, vcc, 0, v5, vcc
	s_waitcnt lgkmcnt(0)
	global_store_dwordx2 v[14:15], v[12:13], off
	v_lshl_add_u64 v[2:3], v[4:5], 0, s[12:13]
	v_lshl_add_u64 v[20:21], v[4:5], 0, s[26:27]
	v_lshl_add_u64 v[22:23], v[4:5], 0, s[28:29]
	v_lshl_add_u64 v[24:25], v[4:5], 0, s[30:31]
	s_andn2_b64 vcc, exec, s[98:99]
	v_pk_mul_f32 v[14:15], v[194:195], s[22:23] op_sel_hi:[1,0]
	v_pk_mul_f32 v[12:13], v[192:193], s[22:23] op_sel_hi:[1,0]
	v_pk_mul_f32 v[16:17], v[196:197], s[22:23] op_sel_hi:[1,0]
	v_pk_fma_f32 v[26:27], v[104:105], s[24:25], v[14:15] op_sel_hi:[1,0,1]
	v_pk_fma_f32 v[28:29], v[102:103], s[24:25], v[12:13] op_sel_hi:[1,0,1]
	v_pk_fma_f32 v[32:33], v[94:95], s[24:25], v[16:17] op_sel_hi:[1,0,1]
	v_med3_f32 v28, v28, s74, v215
	v_med3_f32 v29, v29, s74, v215
	v_med3_f32 v90, v26, s74, v215
	v_med3_f32 v91, v27, s74, v215
	v_cvt_pk_fp8_f32 v26, v28, v29
	v_med3_f32 v28, v32, s74, v215
	v_med3_f32 v29, v33, s74, v215
	v_cvt_pk_fp8_f32 v27, v28, v29
	v_pk_mul_f32 v[18:19], v[198:199], s[22:23] op_sel_hi:[1,0]
	v_pk_fma_f32 v[82:83], v[82:83], s[24:25], v[16:17] op_sel_hi:[1,0,1]
	v_pk_fma_f32 v[30:31], v[96:97], s[24:25], v[18:19] op_sel_hi:[1,0,1]
	v_pk_fma_f32 v[32:33], v[84:85], s[24:25], v[18:19] op_sel_hi:[1,0,1]
	v_med3_f32 v28, v30, s74, v215
	v_med3_f32 v29, v31, s74, v215
	v_cvt_pk_fp8_f32 v27, v28, v29 op_sel:[0,0,1]
	v_pk_fma_f32 v[28:29], v[88:89], s[24:25], v[14:15] op_sel_hi:[1,0,1]
	ds_bpermute_b32 v27, v250, v27
	v_pk_fma_f32 v[30:31], v[86:87], s[24:25], v[12:13] op_sel_hi:[1,0,1]
	v_med3_f32 v84, v28, s74, v215
	v_med3_f32 v30, v30, s74, v215
	v_med3_f32 v31, v31, s74, v215
	v_med3_f32 v85, v29, s74, v215
	v_cvt_pk_fp8_f32 v28, v30, v31
	v_med3_f32 v30, v82, s74, v215
	v_med3_f32 v31, v83, s74, v215
	v_cvt_pk_fp8_f32 v29, v30, v31
	v_med3_f32 v30, v32, s74, v215
	v_med3_f32 v31, v33, s74, v215
	v_pk_fma_f32 v[32:33], v[78:79], s[24:25], v[12:13] op_sel_hi:[1,0,1]
	v_cvt_pk_fp8_f32 v29, v30, v31 op_sel:[0,0,1]
	v_pk_fma_f32 v[30:31], v[80:81], s[24:25], v[14:15] op_sel_hi:[1,0,1]
	ds_bpermute_b32 v29, v250, v29
	v_pk_fma_f32 v[74:75], v[74:75], s[24:25], v[16:17] op_sel_hi:[1,0,1]
	v_med3_f32 v32, v32, s74, v215
	v_med3_f32 v33, v33, s74, v215
	v_med3_f32 v78, v30, s74, v215
	v_med3_f32 v79, v31, s74, v215
	v_cvt_pk_fp8_f32 v30, v32, v33
	v_med3_f32 v32, v74, s74, v215
	v_med3_f32 v33, v75, s74, v215
	v_cvt_pk_fp8_f32 v31, v32, v33
	v_pk_fma_f32 v[76:77], v[76:77], s[24:25], v[18:19] op_sel_hi:[1,0,1]
	v_pk_fma_f32 v[70:71], v[70:71], s[24:25], v[12:13] op_sel_hi:[1,0,1]
	v_med3_f32 v32, v76, s74, v215
	v_med3_f32 v33, v77, s74, v215
	v_cvt_pk_fp8_f32 v31, v32, v33 op_sel:[0,0,1]
	v_pk_fma_f32 v[32:33], v[72:73], s[24:25], v[14:15] op_sel_hi:[1,0,1]
	ds_bpermute_b32 v31, v250, v31
	v_pk_fma_f32 v[66:67], v[66:67], s[24:25], v[16:17] op_sel_hi:[1,0,1]
	v_med3_f32 v70, v70, s74, v215
	v_med3_f32 v71, v71, s74, v215
	v_med3_f32 v72, v32, s74, v215
	v_med3_f32 v73, v33, s74, v215
	v_med3_f32 v66, v66, s74, v215
	v_med3_f32 v67, v67, s74, v215
	v_cvt_pk_fp8_f32 v32, v70, v71
	v_cvt_pk_fp8_f32 v33, v66, v67
	v_cvt_pk_fp8_f32 v26, v90, v91 op_sel:[0,0,1]
	v_cvt_pk_fp8_f32 v28, v84, v85 op_sel:[0,0,1]
	ds_bpermute_b32 v26, v250, v26
	v_pk_fma_f32 v[68:69], v[68:69], s[24:25], v[18:19] op_sel_hi:[1,0,1]
	ds_bpermute_b32 v28, v250, v28
	v_cvt_pk_fp8_f32 v30, v78, v79 op_sel:[0,0,1]
	v_med3_f32 v66, v68, s74, v215
	ds_bpermute_b32 v30, v250, v30
	v_med3_f32 v67, v69, s74, v215
	v_cvt_pk_fp8_f32 v32, v72, v73 op_sel:[0,0,1]
	v_cvt_pk_fp8_f32 v33, v66, v67 op_sel:[0,0,1]
	ds_bpermute_b32 v32, v250, v32
	s_nop 0
	ds_bpermute_b32 v33, v250, v33
	s_waitcnt lgkmcnt(0)
	global_store_dwordx2 v[4:5], v[26:27], off offset:128
	global_store_dwordx2 v[6:7], v[28:29], off offset:128
	global_store_dwordx2 v[8:9], v[30:31], off offset:128
	global_store_dwordx2 v[10:11], v[32:33], off offset:128
	v_pk_fma_f32 v[4:5], v[64:65], s[24:25], v[14:15] op_sel_hi:[1,0,1]
	v_pk_fma_f32 v[6:7], v[62:63], s[24:25], v[12:13] op_sel_hi:[1,0,1]
	v_pk_fma_f32 v[10:11], v[58:59], s[24:25], v[16:17] op_sel_hi:[1,0,1]
	v_med3_f32 v6, v6, s74, v215
	v_med3_f32 v7, v7, s74, v215
	v_med3_f32 v26, v4, s74, v215
	v_med3_f32 v27, v5, s74, v215
	v_cvt_pk_fp8_f32 v4, v6, v7
	v_med3_f32 v6, v10, s74, v215
	v_med3_f32 v7, v11, s74, v215
	v_cvt_pk_fp8_f32 v5, v6, v7
	v_pk_fma_f32 v[8:9], v[60:61], s[24:25], v[18:19] op_sel_hi:[1,0,1]
	v_cvt_pk_fp8_f32 v4, v26, v27 op_sel:[0,0,1]
	v_med3_f32 v6, v8, s74, v215
	ds_bpermute_b32 v4, v250, v4
	v_med3_f32 v7, v9, s74, v215
	v_cvt_pk_fp8_f32 v5, v6, v7 op_sel:[0,0,1]
	v_pk_fma_f32 v[6:7], v[56:57], s[24:25], v[14:15] op_sel_hi:[1,0,1]
	ds_bpermute_b32 v5, v250, v5
	v_pk_fma_f32 v[8:9], v[54:55], s[24:25], v[12:13] op_sel_hi:[1,0,1]
	v_pk_fma_f32 v[26:27], v[50:51], s[24:25], v[16:17] op_sel_hi:[1,0,1]
	v_med3_f32 v8, v8, s74, v215
	v_med3_f32 v9, v9, s74, v215
	v_med3_f32 v28, v6, s74, v215
	v_med3_f32 v29, v7, s74, v215
	v_cvt_pk_fp8_f32 v6, v8, v9
	v_med3_f32 v8, v26, s74, v215
	v_med3_f32 v9, v27, s74, v215
	v_cvt_pk_fp8_f32 v7, v8, v9
	v_pk_fma_f32 v[10:11], v[52:53], s[24:25], v[18:19] op_sel_hi:[1,0,1]
	v_cvt_pk_fp8_f32 v6, v28, v29 op_sel:[0,0,1]
	v_med3_f32 v8, v10, s74, v215
	ds_bpermute_b32 v6, v250, v6
	v_med3_f32 v9, v11, s74, v215
	v_cvt_pk_fp8_f32 v7, v8, v9 op_sel:[0,0,1]
	v_pk_fma_f32 v[8:9], v[48:49], s[24:25], v[14:15] op_sel_hi:[1,0,1]
	ds_bpermute_b32 v7, v250, v7
	v_pk_fma_f32 v[10:11], v[46:47], s[24:25], v[12:13] op_sel_hi:[1,0,1]
	v_pk_fma_f32 v[28:29], v[42:43], s[24:25], v[16:17] op_sel_hi:[1,0,1]
	v_med3_f32 v10, v10, s74, v215
	v_med3_f32 v11, v11, s74, v215
	v_med3_f32 v30, v8, s74, v215
	v_med3_f32 v31, v9, s74, v215
	v_cvt_pk_fp8_f32 v8, v10, v11
	v_med3_f32 v10, v28, s74, v215
	v_med3_f32 v11, v29, s74, v215
	v_cvt_pk_fp8_f32 v9, v10, v11
	v_pk_fma_f32 v[26:27], v[44:45], s[24:25], v[18:19] op_sel_hi:[1,0,1]
	v_pk_fma_f32 v[12:13], v[38:39], s[24:25], v[12:13] op_sel_hi:[1,0,1]
	v_med3_f32 v10, v26, s74, v215
	v_med3_f32 v11, v27, s74, v215
	v_cvt_pk_fp8_f32 v9, v10, v11 op_sel:[0,0,1]
	v_pk_fma_f32 v[10:11], v[40:41], s[24:25], v[14:15] op_sel_hi:[1,0,1]
	ds_bpermute_b32 v9, v250, v9
	v_pk_fma_f32 v[14:15], v[36:37], s[24:25], v[18:19] op_sel_hi:[1,0,1]
	v_pk_fma_f32 v[16:17], v[34:35], s[24:25], v[16:17] op_sel_hi:[1,0,1]
	v_med3_f32 v12, v12, s74, v215
	v_med3_f32 v13, v13, s74, v215
	v_med3_f32 v18, v10, s74, v215
	v_med3_f32 v19, v11, s74, v215
	v_cvt_pk_fp8_f32 v10, v12, v13
	v_med3_f32 v12, v16, s74, v215
	v_med3_f32 v13, v17, s74, v215
	v_cvt_pk_fp8_f32 v11, v12, v13
	v_cvt_pk_fp8_f32 v8, v30, v31 op_sel:[0,0,1]
	v_med3_f32 v12, v14, s74, v215
	ds_bpermute_b32 v8, v250, v8
	v_med3_f32 v13, v15, s74, v215
	v_cvt_pk_fp8_f32 v10, v18, v19 op_sel:[0,0,1]
	v_cvt_pk_fp8_f32 v11, v12, v13 op_sel:[0,0,1]
	ds_bpermute_b32 v10, v250, v10
	s_nop 0
	ds_bpermute_b32 v11, v250, v11
	s_waitcnt lgkmcnt(0)
	global_store_dwordx2 v[2:3], v[4:5], off offset:128
	global_store_dwordx2 v[20:21], v[6:7], off offset:128
	global_store_dwordx2 v[22:23], v[8:9], off offset:128
	global_store_dwordx2 v[24:25], v[10:11], off offset:128
	s_cbranch_vccnz .LBB0_871
	s_branch .Lp7_entry_pre
